# QKV epilogue: RoPE cos/sin tables staged once per phase in 16 KiB static LDS, read by ds_read_b128 (no vmcnt(0) behind the stores of the previous step)
# speedup vs baseline: 1.0088x; 1.0010x over previous
; __device__ __forceinline__ int opaque_tid(int wave) { int l; asm volatile("v_mbcnt_lo_u32_b32 %0, -1, 0\n\tv_mbcnt_hi_u32_b32 %0, -1, %0" : "=v"(l)); return wave * 64 + l; }
; template <class Epi, class Sched, bool ALIGN_EPI, bool FP8 = false>
; __device__ __forceinline__ void gemm_phase(LAS unsigned char* lds, const bf16_t* A, const bf16_t* Bt, const int K, const Sched& S, const Epi& E, const int wave_in) {
;     const int tid = opaque_tid(wave_in); const int wid = __builtin_amdgcn_readfirstlane(tid >> 6), lane = tid & 63, wr = wid >> 2, wc = wid & 3, fr = lane & 15, fq = lane >> 4;
;     const int nt = K / BK;
;     int sR[2], sC[2]; unsigned voffB[2];
; #pragma unroll
;     for (int i = 0; i < 2; ++i) { stage_rc(tid * 16 + i * 8192, sR[i], sC[i]); const int Rb = Epi::PERM ? ((sR[i] & ~31) + perm32(sR[i] & 31)) : sR[i];
;         voffB[i] = (unsigned)(Rb * K + sC[i]) * 2u; }
;     const size_t kstep = (size_t)(BK * 2);
;     const size_t hstep = (size_t)HALF * K * 2;
;     const unsigned ldsw = (unsigned)wid * 1024u;
;     const unsigned ldsbase = (unsigned)__builtin_amdgcn_readfirstlane((int)((unsigned)(uintptr_t)lds + ldsw));
;     const int aoff = lds_byte(wr * 64 + fr, fq * 8), boff = lds_byte(wc * 32 + fr, fq * 8);
;     ...
;     Unit cur, nxt; int ui = 0;
;     if (!S.next(0, cur)) return;
;     f32x4 acc[2][2][4][2];
; #pragma unroll
;     for (int a = 0; a < 2; ++a)
; #pragma unroll
;         for (int b = 0; b < 2; ++b)
; #pragma unroll
;             for (int m = 0; m < 4; ++m)
; #pragma unroll
;                 for (int n = 0; n < 2; ++n) acc[a][b][m][n] = (f32x4){0.f, 0.f, 0.f, 0.f};
;     bf16x8 At[4][2], B0[2][2], B1[2][2];
;     const int sclW = W8_E8M0, sclA = A8_E8M0;
;     unsigned vA[2][2], vN[2][2];
;     PG8_AOFF(vA, cur);
;     const char* const cA = (const char*)A;
;     const char* cB = (const char*)Bt + S.b_off(cur) * 2;
;     PG8_STAGE(PG8_SB(0, 0), cB, voffB[0], voffB[1]); PG8_STAGE(PG8_SB(0, 1), cB + hstep, voffB[0], voffB[1]); PG8_STAGE(PG8_SA(0, 0), cA, vA[0][0], vA[0][1]); PG8_STAGE(PG8_SA(0, 1), cA, vA[1][0], vA[1][1]);
;     if (wr == 1) PG8_BAR;
;     PG8_WAIT_V(2); PG8_BAR;
;     PG8_STAGE(PG8_SB(1, 0), cB + kstep, voffB[0], voffB[1]); PG8_STAGE(PG8_SA(1, 0), cA + kstep, vA[0][0], vA[0][1]); PG8_STAGE(PG8_SB(1, 1), cB + hstep + kstep, voffB[0], voffB[1]);
;     PG8_WAIT_V(6); PG8_BAR;
.LBB0_407:
	s_add_u32 s84, s94, 0x200000
	s_addc_u32 s85, s95, 0
	s_add_u32 s86, s94, 0x202000
	s_addc_u32 s87, s95, 0
	v_mbcnt_lo_u32_b32 v248, -1, 0
	v_mbcnt_hi_u32_b32 v248, -1, v248
	v_lshl_add_u32 v248, s2, 6, v248
	v_lshlrev_b32_e32 v248, 5, v248
	global_load_dwordx4 v[240:243], v248, s[84:85]
	global_load_dwordx4 v[244:247], v248, s[84:85] offset:16
	s_waitcnt vmcnt(0)
	v_add_u32_e32 v248, 0x24000, v248
	ds_write_b128 v248, v[240:243]
	ds_write_b128 v248, v[244:247] offset:16
	s_waitcnt lgkmcnt(0)
	v_bfe_u32 v166, v2, 4, 2
	s_add_u32 s88, s94, 0x76800000
	v_and_b32_e32 v165, 15, v2
	v_lshlrev_b32_e32 v3, 4, v166
	v_lshlrev_b32_e32 v2, 2, v2
	s_addc_u32 s89, s95, 0
	s_and_b32 s5, s2, 3
	s_lshl_b32 s51, s0, 6
	v_lshl_or_b32 v3, v165, 6, v3
	s_lshl_b32 s0, s0, 13
	v_and_b32_e32 v2, 32, v2
	v_bitop3_b32 v4, v3, s0, v2 bitop3:0xde
	s_lshl_b32 s52, s5, 5
	s_lshl_b32 s0, s5, 12
	v_bitop3_b32 v2, v3, s0, v2 bitop3:0xde
	s_add_u32 s0, s10, 0x80
	s_waitcnt vmcnt(2)
	s_barrier
	s_addc_u32 s1, s11, 0
	s_add_i32 s53, s18, 0x18000
	s_mov_b32 m0, s53
	s_nop 0
	global_load_lds_dwordx4 v147, s[0:1]
	s_add_i32 s54, s18, 0x1a000
	s_mov_b32 m0, s54
	s_nop 0
	global_load_lds_dwordx4 v164, s[0:1]
	s_add_u32 s0, s94, 0x99000080
	v_writelane_b32 v232, s92, 18
	s_addc_u32 s1, s95, 0
	s_add_i32 s55, s18, 0x8000
	s_mov_b32 m0, s55
	s_nop 0
	global_load_lds_dwordx4 v173, s[0:1]
	s_add_i32 s56, s18, 0xa000
	s_mov_b32 m0, s56
	s_nop 0
	global_load_lds_dwordx4 v0, s[0:1]
	s_add_u32 s0, s10, 0x20080
	s_addc_u32 s1, s11, 0
	s_add_i32 s57, s18, 0x1c000
	s_mov_b32 m0, s57
	s_nop 0
	global_load_lds_dwordx4 v147, s[0:1]
	s_add_i32 s58, s18, 0x1e000
	s_mov_b32 m0, s58
	s_nop 0
	global_load_lds_dwordx4 v164, s[0:1]
	s_add_i32 s59, s18, 0xc000
	s_add_i32 s64, s18, 0xe000
	s_waitcnt vmcnt(6)
	s_cmpk_lt_u32 s4, 0x100
	v_writelane_b32 v232, s93, 19
	s_cselect_b64 s[90:91], -1, 0
	s_bitcmp0_b32 s4, 6
	v_writelane_b32 v232, s94, 20
	s_mov_b32 s65, 0
	s_cselect_b64 s[2:3], -1, 0
	s_lshl_b32 s66, s5, 11
	s_bfe_u32 s67, s4, 0x20008
	s_ashr_i32 s72, s29, 31
	s_ashr_i32 s73, s38, 31
	s_mov_b32 s81, s19
	s_lshr_b32 s97, s80, 3
	v_add_u32_e32 v167, 0, v2
	v_add_u32_e32 v168, 0, v4
	s_movk_i32 s47, 0x7ff
	v_writelane_b32 v232, s95, 21
	s_barrier
	s_branch .LBB0_410

; __device__ __forceinline__ unsigned cvt_fp8x4_sat(float a, float b, float c, float d) { return cvt_fp8x4(__builtin_amdgcn_fmed3f(a, -448.f, 448.f), __builtin_amdgcn_fmed3f(b, -448.f, 448.f), __builtin_amdgcn_fmed3f(c, -448.f, 448.f), __builtin_amdgcn_fmed3f(d, -448.f, 448.f)); }
;     __device__ __forceinline__ void operator()(const f32x4 (&acc)[2][2][4][2], const Unit& u, int wr, int wc, int fr, int fq, const LAS unsigned char* epl) const {
;     ...
;         bf16_t* base = Q + (size_t)t * qkv_stride;
; #pragma unroll
;         for (int ai = 0; ai < 2; ++ai)
; #pragma unroll
;             for (int m = 0; m < 4; ++m) {
;                 const int row = u.pm * BM + ai * HALF + wr * 64 + m * 16 + fr;
;                 f32x4 cs = (f32x4){1.f, 1.f, 1.f, 1.f}, sn = (f32x4){0.f, 0.f, 0.f, 0.f};
;                 if (row >= NCTX) { const int tp = (row - NCTX) & (SEQ - 1); const int pos = (wc & 1) ? (tp & 63) : (tp >> 6);
;                     cs = *(const f32x4*)(ropec + pos * 16 + 4 * fq); sn = *(const f32x4*)(ropes + pos * 16 + 4 * fq); }
; #pragma unroll
;                 for (int bj = 0; bj < 2; ++bj) { const f32x4 x1 = acc[ai][bj][m][0], x2 = acc[ai][bj][m][1];
;                     f32x4 o1 = x1 * cs - x2 * sn, o2 = x1 * sn + x2 * cs;
;                     if (t == 0) { o1 = o1 * QK_PRESCALE; o2 = o2 * QK_PRESCALE; }
;                     { unsigned char* r8 = (unsigned char*)base + (size_t)row * DM + colt + wc * 32 + 4 * fq + bj * HALF;
;                         *(unsigned*)r8 = cvt_fp8x4_sat(o1[0], o1[1], o1[2], o1[3]); *(unsigned*)(r8 + 16) = cvt_fp8x4_sat(o2[0], o2[1], o2[2], o2[3]); } } }
.LBB0_421:
	s_lshl_b32 s0, s28, 8
	v_lshlrev_b32_e32 v4, 2, v25
	s_add_i32 s0, s0, s51
	v_ashrrev_i32_e32 v5, 31, v4
	v_add_u32_e32 v16, s0, v24
	v_lshlrev_b64 v[2:3], 2, v[4:5]
	v_add_u32_e32 v250, 0x24000, v2
	v_and_b32_e32 v28, 63, v24
	v_lshl_add_u64 v[18:19], s[84:85], 0, v[2:3]
	v_lshl_add_u64 v[20:21], s[86:87], 0, v[2:3]
	v_cmp_lt_i32_e32 vcc, s47, v16
	v_mov_b32_e32 v6, 0
	v_mov_b32_e32 v2, 1.0
	v_mov_b32_e32 v8, 1.0
	v_mov_b32_e32 v9, 1.0
	v_mov_b32_e32 v10, 1.0
	v_mov_b32_e32 v11, 1.0
	v_mov_b32_e32 v12, 0
	v_mov_b32_e32 v13, 0
	v_mov_b32_e32 v14, 0
	v_mov_b32_e32 v15, 0
	s_and_saveexec_b64 s[0:1], vcc
	s_cbranch_execz .LBB0_423
	v_add_u32_e32 v0, 0x1800, v16
	v_bfe_u32 v0, v0, 6, 7
	v_cndmask_b32_e64 v0, v28, v0, s[2:3]
	v_lshlrev_b32_e32 v0, 6, v0
	v_add_u32_e32 v249, v250, v0
	ds_read_b128 v[8:11], v249
	ds_read_b128 v[12:15], v249 offset:8192
.LBB0_423:
	s_or_b64 exec, exec, s[0:1]
	s_lshl_b32 s0, s96, 8
	s_and_b32 s0, s0, 0x300
	s_mul_hi_i32 s1, s6, 0x8400000
	s_mul_i32 s6, s6, 0x8400000
	s_add_u32 s6, s78, s6
	s_addc_u32 s1, s79, s1
	s_cmp_lt_u32 s96, 4
	s_cselect_b64 vcc, -1, 0
	s_add_u32 s0, s6, s0
	s_waitcnt lgkmcnt(0)
	v_pk_mul_f32 v[22:23], v[144:145], v[14:15]
	s_addc_u32 s1, s1, 0
	v_pk_mul_f32 v[174:175], v[142:143], v[12:13]
	v_pk_fma_f32 v[30:31], v[162:163], v[10:11], v[22:23] neg_lo:[0,0,1] neg_hi:[0,0,1]
	s_add_u32 s0, s0, s52
	v_pk_fma_f32 v[174:175], v[160:161], v[8:9], v[174:175] neg_lo:[0,0,1] neg_hi:[0,0,1]
	v_pk_mul_f32 v[178:179], v[160:161], v[12:13]
	v_pk_mul_f32 v[32:33], v[30:31], s[30:31] op_sel_hi:[1,0]
	s_addc_u32 s1, s1, 0
	v_add_u32_e32 v0, 16, v24
	v_ashrrev_i32_e32 v17, 31, v16
	v_pk_fma_f32 v[178:179], v[142:143], v[8:9], v[178:179]
	v_pk_mul_f32 v[180:181], v[174:175], s[30:31] op_sel_hi:[1,0]
	v_lshl_add_u64 v[22:23], s[0:1], 0, v[4:5]
	v_and_b32_e32 v27, 63, v0
	v_lshlrev_b64 v[4:5], 10, v[16:17]
	v_pk_mul_f32 v[198:199], v[178:179], s[30:31] op_sel_hi:[1,0]
	v_cndmask_b32_e32 v0, v31, v33, vcc
	v_cndmask_b32_e32 v3, v30, v32, vcc
	v_cndmask_b32_e32 v7, v175, v181, vcc
	v_cndmask_b32_e32 v17, v174, v180, vcc
	v_pk_mul_f32 v[32:33], v[110:111], v[12:13]
	v_cndmask_b32_e32 v30, v179, v199, vcc
	v_cndmask_b32_e32 v31, v178, v198, vcc
	v_med3_f32 v17, v17, s63, v193
	v_med3_f32 v7, v7, s63, v193
	v_mov_b32_e32 v173, v1
	v_pk_fma_f32 v[32:33], v[126:127], v[8:9], v[32:33] neg_lo:[0,0,1] neg_hi:[0,0,1]
	v_pk_mul_f32 v[12:13], v[126:127], v[12:13]
	v_pk_mul_f32 v[176:177], v[162:163], v[14:15]
	v_cvt_pk_fp8_f32 v173, v17, v7
	v_med3_f32 v7, v31, s63, v193
	v_med3_f32 v17, v30, s63, v193
	v_mov_b32_e32 v178, v1
	v_pk_fma_f32 v[8:9], v[110:111], v[8:9], v[12:13]
	v_pk_mul_f32 v[12:13], v[32:33], s[30:31] op_sel_hi:[1,0]
	v_pk_fma_f32 v[176:177], v[144:145], v[10:11], v[176:177]
	v_cvt_pk_fp8_f32 v178, v7, v17
	v_pk_mul_f32 v[174:175], v[8:9], s[30:31] op_sel_hi:[1,0]
	v_cndmask_b32_e32 v7, v33, v13, vcc
	v_cndmask_b32_e32 v12, v32, v12, vcc
	v_pk_mul_f32 v[200:201], v[176:177], s[30:31] op_sel_hi:[1,0]
	v_pk_mul_f32 v[30:31], v[112:113], v[14:15]
	v_cndmask_b32_e32 v9, v9, v175, vcc
	v_cndmask_b32_e32 v8, v8, v174, vcc
	v_med3_f32 v12, v12, s63, v193
	v_med3_f32 v7, v7, s63, v193
	v_mov_b32_e32 v13, v1
	v_cndmask_b32_e32 v26, v177, v201, vcc
	v_cndmask_b32_e32 v29, v176, v200, vcc
	v_med3_f32 v3, v3, s63, v193
	v_med3_f32 v0, v0, s63, v193
	v_pk_fma_f32 v[30:31], v[128:129], v[10:11], v[30:31] neg_lo:[0,0,1] neg_hi:[0,0,1]
	v_pk_mul_f32 v[14:15], v[128:129], v[14:15]
	v_cvt_pk_fp8_f32 v13, v12, v7
	v_med3_f32 v7, v8, s63, v193
	v_med3_f32 v8, v9, s63, v193
	v_mov_b32_e32 v9, v1
	v_cvt_pk_fp8_f32 v173, v3, v0 op_sel:[0,0,1]
	v_med3_f32 v0, v29, s63, v193
	v_med3_f32 v3, v26, s63, v193
	v_pk_fma_f32 v[10:11], v[112:113], v[10:11], v[14:15]
	v_pk_mul_f32 v[14:15], v[30:31], s[30:31] op_sel_hi:[1,0]
	v_cvt_pk_fp8_f32 v9, v7, v8
	v_cvt_pk_fp8_f32 v178, v0, v3 op_sel:[0,0,1]
	v_pk_mul_f32 v[176:177], v[10:11], s[30:31] op_sel_hi:[1,0]
	v_cndmask_b32_e32 v0, v31, v15, vcc
	v_cndmask_b32_e32 v3, v30, v14, vcc
	v_cndmask_b32_e32 v11, v11, v177, vcc
	v_cndmask_b32_e32 v10, v10, v176, vcc
	v_med3_f32 v3, v3, s63, v193
	v_med3_f32 v0, v0, s63, v193
	v_cvt_pk_fp8_f32 v13, v3, v0 op_sel:[0,0,1]
	v_med3_f32 v0, v10, s63, v193
	v_med3_f32 v3, v11, s63, v193
	v_lshl_add_u64 v[4:5], v[22:23], 0, v[4:5]
	v_cvt_pk_fp8_f32 v9, v0, v3 op_sel:[0,0,1]
	v_add_u32_e32 v10, 16, v16
	global_store_dword v[4:5], v173, off
	global_store_dword v[4:5], v178, off offset:16
	global_store_dword v[4:5], v13, off offset:128
	global_store_dword v[4:5], v9, off offset:144
	v_cmp_lt_i32_e64 s[6:7], s47, v10
	v_mov_b32_e32 v3, 1.0
	v_mov_b32_e32 v4, 1.0
	v_mov_b32_e32 v5, 1.0
	v_mov_b32_e32 v7, 0
	v_mov_b32_e32 v8, 0
	v_mov_b32_e32 v9, 0
	s_and_saveexec_b64 s[0:1], s[6:7]
	s_cbranch_execz .LBB0_425
	v_add_u32_e32 v0, 0x1810, v16
	v_bfe_u32 v0, v0, 6, 7
	v_cndmask_b32_e64 v0, v27, v0, s[2:3]
	v_lshlrev_b32_e32 v0, 6, v0
	v_add_u32_e32 v249, v250, v0
	ds_read_b128 v[2:5], v249
	ds_read_b128 v[6:9], v249 offset:8192
; __device__ __forceinline__ unsigned cvt_fp8x4_sat(float a, float b, float c, float d) { return cvt_fp8x4(__builtin_amdgcn_fmed3f(a, -448.f, 448.f), __builtin_amdgcn_fmed3f(b, -448.f, 448.f), __builtin_amdgcn_fmed3f(c, -448.f, 448.f), __builtin_amdgcn_fmed3f(d, -448.f, 448.f)); }
;     __device__ __forceinline__ void operator()(const f32x4 (&acc)[2][2][4][2], const Unit& u, int wr, int wc, int fr, int fq, const LAS unsigned char* epl) const {
;     ...
;         bf16_t* base = Q + (size_t)t * qkv_stride;
; #pragma unroll
;         for (int ai = 0; ai < 2; ++ai)
; #pragma unroll
;             for (int m = 0; m < 4; ++m) {
;                 const int row = u.pm * BM + ai * HALF + wr * 64 + m * 16 + fr;
;                 f32x4 cs = (f32x4){1.f, 1.f, 1.f, 1.f}, sn = (f32x4){0.f, 0.f, 0.f, 0.f};
;                 if (row >= NCTX) { const int tp = (row - NCTX) & (SEQ - 1); const int pos = (wc & 1) ? (tp & 63) : (tp >> 6);
;                     cs = *(const f32x4*)(ropec + pos * 16 + 4 * fq); sn = *(const f32x4*)(ropes + pos * 16 + 4 * fq); }
; #pragma unroll
;                 for (int bj = 0; bj < 2; ++bj) { const f32x4 x1 = acc[ai][bj][m][0], x2 = acc[ai][bj][m][1];
;                     f32x4 o1 = x1 * cs - x2 * sn, o2 = x1 * sn + x2 * cs;
;                     if (t == 0) { o1 = o1 * QK_PRESCALE; o2 = o2 * QK_PRESCALE; }
;                     { unsigned char* r8 = (unsigned char*)base + (size_t)row * DM + colt + wc * 32 + 4 * fq + bj * HALF;
;                         *(unsigned*)r8 = cvt_fp8x4_sat(o1[0], o1[1], o1[2], o1[3]); *(unsigned*)(r8 + 16) = cvt_fp8x4_sat(o2[0], o2[1], o2[2], o2[3]); } } }
.LBB0_425:
	s_or_b64 exec, exec, s[0:1]
	s_waitcnt lgkmcnt(0)
	v_pk_mul_f32 v[12:13], v[140:141], v[8:9]
	v_pk_mul_f32 v[14:15], v[138:139], v[6:7]
	v_pk_fma_f32 v[12:13], v[158:159], v[4:5], v[12:13] neg_lo:[0,0,1] neg_hi:[0,0,1]
	v_pk_fma_f32 v[14:15], v[156:157], v[2:3], v[14:15] neg_lo:[0,0,1] neg_hi:[0,0,1]
	v_pk_mul_f32 v[30:31], v[158:159], v[8:9]
	v_pk_mul_f32 v[32:33], v[156:157], v[6:7]
	v_pk_fma_f32 v[30:31], v[140:141], v[4:5], v[30:31]
	v_pk_fma_f32 v[32:33], v[138:139], v[2:3], v[32:33]
	v_pk_mul_f32 v[174:175], v[14:15], s[30:31] op_sel_hi:[1,0]
	v_pk_mul_f32 v[176:177], v[12:13], s[30:31] op_sel_hi:[1,0]
	v_pk_mul_f32 v[178:179], v[32:33], s[30:31] op_sel_hi:[1,0]
	v_pk_mul_f32 v[180:181], v[30:31], s[30:31] op_sel_hi:[1,0]
	v_cndmask_b32_e32 v0, v13, v177, vcc
	v_cndmask_b32_e32 v13, v15, v175, vcc
	v_cndmask_b32_e32 v14, v14, v174, vcc
	v_cndmask_b32_e32 v26, v30, v180, vcc
	v_cndmask_b32_e32 v29, v33, v179, vcc
	v_cndmask_b32_e32 v30, v32, v178, vcc
	v_med3_f32 v14, v14, s63, v193
	v_med3_f32 v13, v13, s63, v193
	v_mov_b32_e32 v173, v1
	v_cvt_pk_fp8_f32 v173, v14, v13
	v_med3_f32 v13, v30, s63, v193
	v_med3_f32 v14, v29, s63, v193
	v_mov_b32_e32 v29, v1
	v_cvt_pk_fp8_f32 v29, v13, v14
	v_cndmask_b32_e32 v12, v12, v176, vcc
	v_cndmask_b32_e32 v15, v31, v181, vcc
	v_med3_f32 v12, v12, s63, v193
	v_med3_f32 v0, v0, s63, v193
	v_cvt_pk_fp8_f32 v173, v12, v0 op_sel:[0,0,1]
	v_med3_f32 v0, v26, s63, v193
	v_med3_f32 v12, v15, s63, v193
	v_pk_mul_f32 v[14:15], v[106:107], v[6:7]
	v_cvt_pk_fp8_f32 v29, v0, v12 op_sel:[0,0,1]
	v_pk_mul_f32 v[12:13], v[108:109], v[8:9]
	v_pk_fma_f32 v[14:15], v[122:123], v[2:3], v[14:15] neg_lo:[0,0,1] neg_hi:[0,0,1]
	v_pk_mul_f32 v[6:7], v[122:123], v[6:7]
	v_pk_fma_f32 v[12:13], v[124:125], v[4:5], v[12:13] neg_lo:[0,0,1] neg_hi:[0,0,1]
	v_pk_mul_f32 v[8:9], v[124:125], v[8:9]
	v_pk_fma_f32 v[2:3], v[106:107], v[2:3], v[6:7]
	v_pk_mul_f32 v[6:7], v[14:15], s[30:31] op_sel_hi:[1,0]
	v_pk_fma_f32 v[4:5], v[108:109], v[4:5], v[8:9]
	v_pk_mul_f32 v[8:9], v[12:13], s[30:31] op_sel_hi:[1,0]
	v_pk_mul_f32 v[30:31], v[2:3], s[30:31] op_sel_hi:[1,0]
	v_cndmask_b32_e32 v7, v15, v7, vcc
	v_cndmask_b32_e32 v6, v14, v6, vcc
	v_cndmask_b32_e32 v0, v13, v9, vcc
	v_cndmask_b32_e32 v3, v3, v31, vcc
	v_cndmask_b32_e32 v2, v2, v30, vcc
	v_med3_f32 v6, v6, s63, v193
	v_med3_f32 v7, v7, s63, v193
	v_mov_b32_e32 v9, v1
	v_cvt_pk_fp8_f32 v9, v6, v7
	v_med3_f32 v2, v2, s63, v193
	v_med3_f32 v3, v3, s63, v193
	v_mov_b32_e32 v6, v1
	v_cvt_pk_fp8_f32 v6, v2, v3
	v_pk_mul_f32 v[32:33], v[4:5], s[30:31] op_sel_hi:[1,0]
	v_cndmask_b32_e32 v8, v12, v8, vcc
	v_ashrrev_i32_e32 v11, 31, v10
	v_cndmask_b32_e32 v5, v5, v33, vcc
	v_cndmask_b32_e32 v4, v4, v32, vcc
	v_med3_f32 v8, v8, s63, v193
	v_med3_f32 v0, v0, s63, v193
	v_lshlrev_b64 v[10:11], 10, v[10:11]
	v_cvt_pk_fp8_f32 v9, v8, v0 op_sel:[0,0,1]
	v_med3_f32 v0, v4, s63, v193
	v_med3_f32 v2, v5, s63, v193
	v_lshl_add_u64 v[10:11], v[22:23], 0, v[10:11]
	v_cvt_pk_fp8_f32 v6, v0, v2 op_sel:[0,0,1]
	v_add_u32_e32 v4, 32, v16
	v_xor_b32_e32 v17, 32, v28
	global_store_dword v[10:11], v173, off
	global_store_dword v[10:11], v29, off offset:16
	global_store_dword v[10:11], v9, off offset:128
	global_store_dword v[10:11], v6, off offset:144
	v_cmp_lt_i32_e64 s[6:7], s47, v4
	v_mov_b32_e32 v6, 0
	v_mov_b32_e32 v2, 1.0
	v_mov_b32_e32 v8, 1.0
	v_mov_b32_e32 v9, 1.0
	v_mov_b32_e32 v10, 1.0
	v_mov_b32_e32 v11, 1.0
	v_mov_b32_e32 v12, 0
	v_mov_b32_e32 v13, 0
	v_mov_b32_e32 v14, 0
	v_mov_b32_e32 v15, 0
	s_and_saveexec_b64 s[0:1], s[6:7]
	s_cbranch_execz .LBB0_427
	v_add_u32_e32 v0, 0x1820, v16
	v_bfe_u32 v0, v0, 6, 7
	v_cndmask_b32_e64 v0, v17, v0, s[2:3]
	v_lshlrev_b32_e32 v0, 6, v0
	v_add_u32_e32 v249, v250, v0
	ds_read_b128 v[8:11], v249
	ds_read_b128 v[12:15], v249 offset:8192
.LBB0_427:
	s_or_b64 exec, exec, s[0:1]
	s_waitcnt lgkmcnt(0)
	v_pk_mul_f32 v[32:33], v[134:135], v[12:13]
	v_pk_mul_f32 v[176:177], v[152:153], v[12:13]
	v_pk_fma_f32 v[32:33], v[152:153], v[8:9], v[32:33] neg_lo:[0,0,1] neg_hi:[0,0,1]
	v_pk_fma_f32 v[176:177], v[134:135], v[8:9], v[176:177]
	v_pk_mul_f32 v[178:179], v[32:33], s[30:31] op_sel_hi:[1,0]
	v_pk_mul_f32 v[198:199], v[176:177], s[30:31] op_sel_hi:[1,0]
	v_cndmask_b32_e32 v7, v33, v179, vcc
	v_cndmask_b32_e32 v29, v32, v178, vcc
	v_pk_mul_f32 v[30:31], v[136:137], v[14:15]
	v_cndmask_b32_e32 v32, v177, v199, vcc
	v_cndmask_b32_e32 v33, v176, v198, vcc
	v_med3_f32 v29, v29, s63, v193
	v_med3_f32 v7, v7, s63, v193
	v_mov_b32_e32 v173, v1
	v_pk_fma_f32 v[30:31], v[154:155], v[10:11], v[30:31] neg_lo:[0,0,1] neg_hi:[0,0,1]
	v_pk_mul_f32 v[174:175], v[154:155], v[14:15]
	v_cvt_pk_fp8_f32 v173, v29, v7
	v_med3_f32 v7, v33, s63, v193
	v_med3_f32 v29, v32, s63, v193
	v_pk_mul_f32 v[32:33], v[102:103], v[12:13]
	v_add_u32_e32 v0, 48, v24
	v_pk_fma_f32 v[174:175], v[136:137], v[10:11], v[174:175]
	v_pk_mul_f32 v[180:181], v[30:31], s[30:31] op_sel_hi:[1,0]
	v_pk_fma_f32 v[32:33], v[118:119], v[8:9], v[32:33] neg_lo:[0,0,1] neg_hi:[0,0,1]
	v_pk_mul_f32 v[12:13], v[118:119], v[12:13]
	v_and_b32_e32 v26, 63, v0
	v_pk_mul_f32 v[200:201], v[174:175], s[30:31] op_sel_hi:[1,0]
	v_cndmask_b32_e32 v0, v31, v181, vcc
	v_cndmask_b32_e32 v3, v30, v180, vcc
	v_mov_b32_e32 v178, v1
	v_pk_fma_f32 v[8:9], v[102:103], v[8:9], v[12:13]
	v_pk_mul_f32 v[12:13], v[32:33], s[30:31] op_sel_hi:[1,0]
	v_cndmask_b32_e32 v30, v175, v201, vcc
	v_cndmask_b32_e32 v31, v174, v200, vcc
	v_med3_f32 v3, v3, s63, v193
	v_med3_f32 v0, v0, s63, v193
	v_cvt_pk_fp8_f32 v178, v7, v29
	v_pk_mul_f32 v[174:175], v[8:9], s[30:31] op_sel_hi:[1,0]
	v_cndmask_b32_e32 v7, v33, v13, vcc
; __device__ __forceinline__ unsigned cvt_fp8x4_sat(float a, float b, float c, float d) { return cvt_fp8x4(__builtin_amdgcn_fmed3f(a, -448.f, 448.f), __builtin_amdgcn_fmed3f(b, -448.f, 448.f), __builtin_amdgcn_fmed3f(c, -448.f, 448.f), __builtin_amdgcn_fmed3f(d, -448.f, 448.f)); }
;     __device__ __forceinline__ void operator()(const f32x4 (&acc)[2][2][4][2], const Unit& u, int wr, int wc, int fr, int fq, const LAS unsigned char* epl) const {
;     ...
;         bf16_t* base = Q + (size_t)t * qkv_stride;
; #pragma unroll
;         for (int ai = 0; ai < 2; ++ai)
; #pragma unroll
;             for (int m = 0; m < 4; ++m) {
;                 const int row = u.pm * BM + ai * HALF + wr * 64 + m * 16 + fr;
;                 f32x4 cs = (f32x4){1.f, 1.f, 1.f, 1.f}, sn = (f32x4){0.f, 0.f, 0.f, 0.f};
;                 if (row >= NCTX) { const int tp = (row - NCTX) & (SEQ - 1); const int pos = (wc & 1) ? (tp & 63) : (tp >> 6);
;                     cs = *(const f32x4*)(ropec + pos * 16 + 4 * fq); sn = *(const f32x4*)(ropes + pos * 16 + 4 * fq); }
; #pragma unroll
;                 for (int bj = 0; bj < 2; ++bj) { const f32x4 x1 = acc[ai][bj][m][0], x2 = acc[ai][bj][m][1];
;                     f32x4 o1 = x1 * cs - x2 * sn, o2 = x1 * sn + x2 * cs;
;                     if (t == 0) { o1 = o1 * QK_PRESCALE; o2 = o2 * QK_PRESCALE; }
;                     { unsigned char* r8 = (unsigned char*)base + (size_t)row * DM + colt + wc * 32 + 4 * fq + bj * HALF;
;                         *(unsigned*)r8 = cvt_fp8x4_sat(o1[0], o1[1], o1[2], o1[3]); *(unsigned*)(r8 + 16) = cvt_fp8x4_sat(o2[0], o2[1], o2[2], o2[3]); } } }
	v_cndmask_b32_e32 v12, v32, v12, vcc
	v_cvt_pk_fp8_f32 v173, v3, v0 op_sel:[0,0,1]
	v_med3_f32 v0, v31, s63, v193
	v_med3_f32 v3, v30, s63, v193
	v_pk_mul_f32 v[30:31], v[104:105], v[14:15]
	v_cndmask_b32_e32 v9, v9, v175, vcc
	v_cndmask_b32_e32 v8, v8, v174, vcc
	v_med3_f32 v12, v12, s63, v193
	v_med3_f32 v7, v7, s63, v193
	v_mov_b32_e32 v13, v1
	v_pk_fma_f32 v[30:31], v[120:121], v[10:11], v[30:31] neg_lo:[0,0,1] neg_hi:[0,0,1]
	v_pk_mul_f32 v[14:15], v[120:121], v[14:15]
	v_cvt_pk_fp8_f32 v13, v12, v7
	v_med3_f32 v7, v8, s63, v193
	v_med3_f32 v8, v9, s63, v193
	v_mov_b32_e32 v9, v1
	v_pk_fma_f32 v[10:11], v[104:105], v[10:11], v[14:15]
	v_pk_mul_f32 v[14:15], v[30:31], s[30:31] op_sel_hi:[1,0]
	v_cvt_pk_fp8_f32 v9, v7, v8
	v_cvt_pk_fp8_f32 v178, v0, v3 op_sel:[0,0,1]
	v_pk_mul_f32 v[176:177], v[10:11], s[30:31] op_sel_hi:[1,0]
	v_cndmask_b32_e32 v0, v31, v15, vcc
	v_cndmask_b32_e32 v3, v30, v14, vcc
	v_ashrrev_i32_e32 v5, 31, v4
	v_cndmask_b32_e32 v11, v11, v177, vcc
	v_cndmask_b32_e32 v10, v10, v176, vcc
	v_med3_f32 v3, v3, s63, v193
	v_med3_f32 v0, v0, s63, v193
	v_lshlrev_b64 v[4:5], 10, v[4:5]
	v_cvt_pk_fp8_f32 v13, v3, v0 op_sel:[0,0,1]
	v_med3_f32 v0, v10, s63, v193
	v_med3_f32 v3, v11, s63, v193
	v_lshl_add_u64 v[4:5], v[22:23], 0, v[4:5]
	v_cvt_pk_fp8_f32 v9, v0, v3 op_sel:[0,0,1]
	v_add_u32_e32 v10, 48, v16
	global_store_dword v[4:5], v173, off
	global_store_dword v[4:5], v178, off offset:16
	global_store_dword v[4:5], v13, off offset:128
	global_store_dword v[4:5], v9, off offset:144
	v_cmp_lt_i32_e64 s[6:7], s47, v10
	v_mov_b32_e32 v3, 1.0
	v_mov_b32_e32 v4, 1.0
	v_mov_b32_e32 v5, 1.0
	v_mov_b32_e32 v7, 0
	v_mov_b32_e32 v8, 0
	v_mov_b32_e32 v9, 0
	s_and_saveexec_b64 s[0:1], s[6:7]
	s_cbranch_execz .LBB0_429
	v_add_u32_e32 v0, 0x1830, v16
	v_bfe_u32 v0, v0, 6, 7
	v_cndmask_b32_e64 v0, v26, v0, s[2:3]
	v_lshlrev_b32_e32 v0, 6, v0
	v_add_u32_e32 v249, v250, v0
	ds_read_b128 v[2:5], v249
	ds_read_b128 v[6:9], v249 offset:8192
.LBB0_429:
	s_or_b64 exec, exec, s[0:1]
	s_waitcnt lgkmcnt(0)
	v_pk_mul_f32 v[12:13], v[132:133], v[8:9]
	v_pk_mul_f32 v[14:15], v[130:131], v[6:7]
	v_pk_fma_f32 v[12:13], v[150:151], v[4:5], v[12:13] neg_lo:[0,0,1] neg_hi:[0,0,1]
	v_pk_fma_f32 v[14:15], v[148:149], v[2:3], v[14:15] neg_lo:[0,0,1] neg_hi:[0,0,1]
	v_pk_mul_f32 v[30:31], v[150:151], v[8:9]
	v_pk_mul_f32 v[32:33], v[148:149], v[6:7]
	v_pk_fma_f32 v[30:31], v[132:133], v[4:5], v[30:31]
	v_pk_fma_f32 v[32:33], v[130:131], v[2:3], v[32:33]
	v_pk_mul_f32 v[174:175], v[14:15], s[30:31] op_sel_hi:[1,0]
	v_pk_mul_f32 v[176:177], v[12:13], s[30:31] op_sel_hi:[1,0]
	v_pk_mul_f32 v[178:179], v[32:33], s[30:31] op_sel_hi:[1,0]
	v_pk_mul_f32 v[180:181], v[30:31], s[30:31] op_sel_hi:[1,0]
	v_cndmask_b32_e32 v0, v13, v177, vcc
	v_cndmask_b32_e32 v13, v15, v175, vcc
	v_cndmask_b32_e32 v14, v14, v174, vcc
	v_cndmask_b32_e32 v15, v31, v181, vcc
	v_cndmask_b32_e32 v29, v30, v180, vcc
	v_cndmask_b32_e32 v30, v33, v179, vcc
	v_cndmask_b32_e32 v31, v32, v178, vcc
	v_med3_f32 v14, v14, s63, v193
	v_med3_f32 v13, v13, s63, v193
	v_mov_b32_e32 v173, v1
	v_cvt_pk_fp8_f32 v173, v14, v13
	v_med3_f32 v13, v31, s63, v193
	v_med3_f32 v14, v30, s63, v193
	v_mov_b32_e32 v174, v1
	v_cvt_pk_fp8_f32 v174, v13, v14
	v_cndmask_b32_e32 v12, v12, v176, vcc
	v_med3_f32 v12, v12, s63, v193
	v_med3_f32 v0, v0, s63, v193
	v_cvt_pk_fp8_f32 v173, v12, v0 op_sel:[0,0,1]
	v_med3_f32 v0, v29, s63, v193
	v_med3_f32 v12, v15, s63, v193
	v_pk_mul_f32 v[14:15], v[98:99], v[6:7]
	v_cvt_pk_fp8_f32 v174, v0, v12 op_sel:[0,0,1]
	v_pk_mul_f32 v[12:13], v[100:101], v[8:9]
	v_pk_fma_f32 v[14:15], v[114:115], v[2:3], v[14:15] neg_lo:[0,0,1] neg_hi:[0,0,1]
	v_pk_mul_f32 v[6:7], v[114:115], v[6:7]
	v_pk_fma_f32 v[12:13], v[116:117], v[4:5], v[12:13] neg_lo:[0,0,1] neg_hi:[0,0,1]
	v_pk_mul_f32 v[8:9], v[116:117], v[8:9]
	v_pk_fma_f32 v[2:3], v[98:99], v[2:3], v[6:7]
	v_pk_mul_f32 v[6:7], v[14:15], s[30:31] op_sel_hi:[1,0]
	v_pk_fma_f32 v[4:5], v[100:101], v[4:5], v[8:9]
	v_pk_mul_f32 v[8:9], v[12:13], s[30:31] op_sel_hi:[1,0]
	v_pk_mul_f32 v[30:31], v[2:3], s[30:31] op_sel_hi:[1,0]
	v_cndmask_b32_e32 v7, v15, v7, vcc
	v_cndmask_b32_e32 v6, v14, v6, vcc
	v_cndmask_b32_e32 v0, v13, v9, vcc
	v_cndmask_b32_e32 v3, v3, v31, vcc
	v_cndmask_b32_e32 v2, v2, v30, vcc
	v_med3_f32 v6, v6, s63, v193
	v_med3_f32 v7, v7, s63, v193
	v_mov_b32_e32 v9, v1
	v_cvt_pk_fp8_f32 v9, v6, v7
	v_med3_f32 v2, v2, s63, v193
	v_med3_f32 v3, v3, s63, v193
	v_mov_b32_e32 v6, v1
	v_cvt_pk_fp8_f32 v6, v2, v3
	v_pk_mul_f32 v[32:33], v[4:5], s[30:31] op_sel_hi:[1,0]
	v_cndmask_b32_e32 v8, v12, v8, vcc
	v_ashrrev_i32_e32 v11, 31, v10
	v_cndmask_b32_e32 v5, v5, v33, vcc
	v_cndmask_b32_e32 v4, v4, v32, vcc
	v_med3_f32 v8, v8, s63, v193
	v_med3_f32 v0, v0, s63, v193
	v_lshlrev_b64 v[10:11], 10, v[10:11]
	v_cvt_pk_fp8_f32 v9, v8, v0 op_sel:[0,0,1]
	v_med3_f32 v0, v4, s63, v193
	v_med3_f32 v2, v5, s63, v193
	v_lshl_add_u64 v[10:11], v[22:23], 0, v[10:11]
	v_cvt_pk_fp8_f32 v6, v0, v2 op_sel:[0,0,1]
	v_add_u32_e32 v4, 0x80, v16
	global_store_dword v[10:11], v173, off
	global_store_dword v[10:11], v174, off offset:16
	global_store_dword v[10:11], v9, off offset:128
	global_store_dword v[10:11], v6, off offset:144
	v_cmp_lt_i32_e64 s[6:7], s47, v4
	v_mov_b32_e32 v6, 0
	v_mov_b32_e32 v2, 1.0
	v_mov_b32_e32 v8, 1.0
	v_mov_b32_e32 v9, 1.0
	v_mov_b32_e32 v10, 1.0
	v_mov_b32_e32 v11, 1.0
	v_mov_b32_e32 v12, 0
	v_mov_b32_e32 v13, 0
	v_mov_b32_e32 v14, 0
	v_mov_b32_e32 v15, 0
	s_and_saveexec_b64 s[0:1], s[6:7]
	s_cbranch_execz .LBB0_431
	v_add_u32_e32 v0, 0x1880, v16
	v_bfe_u32 v0, v0, 6, 7
	v_cndmask_b32_e64 v0, v28, v0, s[2:3]
	v_lshlrev_b32_e32 v0, 6, v0
	v_add_u32_e32 v249, v250, v0
	ds_read_b128 v[8:11], v249
	ds_read_b128 v[12:15], v249 offset:8192
; __device__ __forceinline__ unsigned cvt_fp8x4_sat(float a, float b, float c, float d) { return cvt_fp8x4(__builtin_amdgcn_fmed3f(a, -448.f, 448.f), __builtin_amdgcn_fmed3f(b, -448.f, 448.f), __builtin_amdgcn_fmed3f(c, -448.f, 448.f), __builtin_amdgcn_fmed3f(d, -448.f, 448.f)); }
;     __device__ __forceinline__ void operator()(const f32x4 (&acc)[2][2][4][2], const Unit& u, int wr, int wc, int fr, int fq, const LAS unsigned char* epl) const {
;     ...
;         bf16_t* base = Q + (size_t)t * qkv_stride;
; #pragma unroll
;         for (int ai = 0; ai < 2; ++ai)
; #pragma unroll
;             for (int m = 0; m < 4; ++m) {
;                 const int row = u.pm * BM + ai * HALF + wr * 64 + m * 16 + fr;
;                 f32x4 cs = (f32x4){1.f, 1.f, 1.f, 1.f}, sn = (f32x4){0.f, 0.f, 0.f, 0.f};
;                 if (row >= NCTX) { const int tp = (row - NCTX) & (SEQ - 1); const int pos = (wc & 1) ? (tp & 63) : (tp >> 6);
;                     cs = *(const f32x4*)(ropec + pos * 16 + 4 * fq); sn = *(const f32x4*)(ropes + pos * 16 + 4 * fq); }
; #pragma unroll
;                 for (int bj = 0; bj < 2; ++bj) { const f32x4 x1 = acc[ai][bj][m][0], x2 = acc[ai][bj][m][1];
;                     f32x4 o1 = x1 * cs - x2 * sn, o2 = x1 * sn + x2 * cs;
;                     if (t == 0) { o1 = o1 * QK_PRESCALE; o2 = o2 * QK_PRESCALE; }
;                     { unsigned char* r8 = (unsigned char*)base + (size_t)row * DM + colt + wc * 32 + 4 * fq + bj * HALF;
;                         *(unsigned*)r8 = cvt_fp8x4_sat(o1[0], o1[1], o1[2], o1[3]); *(unsigned*)(r8 + 16) = cvt_fp8x4_sat(o2[0], o2[1], o2[2], o2[3]); } } }
.LBB0_431:
	s_or_b64 exec, exec, s[0:1]
	s_waitcnt lgkmcnt(0)
	v_pk_mul_f32 v[28:29], v[80:81], v[14:15]
	v_pk_mul_f32 v[30:31], v[78:79], v[12:13]
	v_pk_fma_f32 v[28:29], v[96:97], v[10:11], v[28:29] neg_lo:[0,0,1] neg_hi:[0,0,1]
	v_pk_fma_f32 v[30:31], v[94:95], v[8:9], v[30:31] neg_lo:[0,0,1] neg_hi:[0,0,1]
	v_pk_mul_f32 v[178:179], v[28:29], s[30:31] op_sel_hi:[1,0]
	v_pk_mul_f32 v[176:177], v[30:31], s[30:31] op_sel_hi:[1,0]
	v_cndmask_b32_e32 v3, v28, v178, vcc
	v_cndmask_b32_e32 v7, v31, v177, vcc
	v_cndmask_b32_e32 v28, v30, v176, vcc
	v_med3_f32 v28, v28, s63, v193
	v_med3_f32 v7, v7, s63, v193
	v_mov_b32_e32 v173, v1
	v_pk_mul_f32 v[32:33], v[96:97], v[14:15]
	v_pk_mul_f32 v[174:175], v[94:95], v[12:13]
	v_cvt_pk_fp8_f32 v173, v28, v7
	v_pk_fma_f32 v[174:175], v[78:79], v[8:9], v[174:175]
	v_pk_fma_f32 v[32:33], v[80:81], v[10:11], v[32:33]
	v_pk_mul_f32 v[180:181], v[174:175], s[30:31] op_sel_hi:[1,0]
	v_pk_mul_f32 v[198:199], v[32:33], s[30:31] op_sel_hi:[1,0]
	v_cndmask_b32_e32 v0, v29, v179, vcc
	v_cndmask_b32_e32 v30, v32, v198, vcc
	v_cndmask_b32_e32 v31, v175, v181, vcc
	v_med3_f32 v3, v3, s63, v193
	v_med3_f32 v0, v0, s63, v193
	v_med3_f32 v28, v31, s63, v193
	v_cvt_pk_fp8_f32 v173, v3, v0 op_sel:[0,0,1]
	v_med3_f32 v0, v30, s63, v193
	v_pk_mul_f32 v[30:31], v[46:47], v[12:13]
	v_cndmask_b32_e32 v32, v174, v180, vcc
	v_pk_fma_f32 v[30:31], v[62:63], v[8:9], v[30:31] neg_lo:[0,0,1] neg_hi:[0,0,1]
	v_pk_mul_f32 v[12:13], v[62:63], v[12:13]
	v_med3_f32 v7, v32, s63, v193
	v_mov_b32_e32 v176, v1
	v_pk_fma_f32 v[8:9], v[46:47], v[8:9], v[12:13]
	v_pk_mul_f32 v[12:13], v[30:31], s[30:31] op_sel_hi:[1,0]
	v_cndmask_b32_e32 v29, v33, v199, vcc
	v_cvt_pk_fp8_f32 v176, v7, v28
	v_pk_mul_f32 v[32:33], v[8:9], s[30:31] op_sel_hi:[1,0]
	v_cndmask_b32_e32 v7, v31, v13, vcc
	v_cndmask_b32_e32 v12, v30, v12, vcc
	v_med3_f32 v3, v29, s63, v193
	v_pk_mul_f32 v[28:29], v[48:49], v[14:15]
	v_cndmask_b32_e32 v9, v9, v33, vcc
	v_cndmask_b32_e32 v8, v8, v32, vcc
	v_med3_f32 v12, v12, s63, v193
	v_med3_f32 v7, v7, s63, v193
	v_mov_b32_e32 v13, v1
	v_pk_fma_f32 v[28:29], v[64:65], v[10:11], v[28:29] neg_lo:[0,0,1] neg_hi:[0,0,1]
	v_pk_mul_f32 v[14:15], v[64:65], v[14:15]
	v_cvt_pk_fp8_f32 v13, v12, v7
	v_med3_f32 v7, v8, s63, v193
	v_med3_f32 v8, v9, s63, v193
	v_mov_b32_e32 v9, v1
	v_pk_fma_f32 v[10:11], v[48:49], v[10:11], v[14:15]
	v_pk_mul_f32 v[14:15], v[28:29], s[30:31] op_sel_hi:[1,0]
	v_cvt_pk_fp8_f32 v9, v7, v8
	v_cvt_pk_fp8_f32 v176, v0, v3 op_sel:[0,0,1]
	v_pk_mul_f32 v[174:175], v[10:11], s[30:31] op_sel_hi:[1,0]
	v_cndmask_b32_e32 v0, v29, v15, vcc
	v_cndmask_b32_e32 v3, v28, v14, vcc
	v_ashrrev_i32_e32 v5, 31, v4
	v_cndmask_b32_e32 v11, v11, v175, vcc
	v_cndmask_b32_e32 v10, v10, v174, vcc
	v_med3_f32 v3, v3, s63, v193
	v_med3_f32 v0, v0, s63, v193
	v_lshlrev_b64 v[4:5], 10, v[4:5]
	v_cvt_pk_fp8_f32 v13, v3, v0 op_sel:[0,0,1]
	v_med3_f32 v0, v10, s63, v193
	v_med3_f32 v3, v11, s63, v193
	v_lshl_add_u64 v[4:5], v[22:23], 0, v[4:5]
	v_cvt_pk_fp8_f32 v9, v0, v3 op_sel:[0,0,1]
	v_add_u32_e32 v10, 0x90, v16
	global_store_dword v[4:5], v173, off
	global_store_dword v[4:5], v176, off offset:16
	global_store_dword v[4:5], v13, off offset:128
	global_store_dword v[4:5], v9, off offset:144
	v_cmp_lt_i32_e64 s[6:7], s47, v10
	v_mov_b32_e32 v3, 1.0
	v_mov_b32_e32 v4, 1.0
	v_mov_b32_e32 v5, 1.0
	v_mov_b32_e32 v7, 0
	v_mov_b32_e32 v8, 0
	v_mov_b32_e32 v9, 0
	s_and_saveexec_b64 s[0:1], s[6:7]
	s_cbranch_execz .LBB0_433
	v_add_u32_e32 v0, 0x1890, v16
	v_bfe_u32 v0, v0, 6, 7
	v_cndmask_b32_e64 v0, v27, v0, s[2:3]
	v_lshlrev_b32_e32 v0, 6, v0
	v_add_u32_e32 v249, v250, v0
	ds_read_b128 v[2:5], v249
	ds_read_b128 v[6:9], v249 offset:8192
.LBB0_433:
	s_or_b64 exec, exec, s[0:1]
	s_waitcnt lgkmcnt(0)
	v_pk_mul_f32 v[12:13], v[76:77], v[8:9]
	v_pk_mul_f32 v[14:15], v[74:75], v[6:7]
	v_pk_fma_f32 v[12:13], v[92:93], v[4:5], v[12:13] neg_lo:[0,0,1] neg_hi:[0,0,1]
	v_pk_fma_f32 v[14:15], v[90:91], v[2:3], v[14:15] neg_lo:[0,0,1] neg_hi:[0,0,1]
	v_pk_mul_f32 v[28:29], v[92:93], v[8:9]
	v_pk_mul_f32 v[30:31], v[90:91], v[6:7]
	v_pk_fma_f32 v[28:29], v[76:77], v[4:5], v[28:29]
	v_pk_fma_f32 v[30:31], v[74:75], v[2:3], v[30:31]
	v_pk_mul_f32 v[32:33], v[14:15], s[30:31] op_sel_hi:[1,0]
	v_pk_mul_f32 v[174:175], v[12:13], s[30:31] op_sel_hi:[1,0]
	v_pk_mul_f32 v[176:177], v[30:31], s[30:31] op_sel_hi:[1,0]
	v_pk_mul_f32 v[178:179], v[28:29], s[30:31] op_sel_hi:[1,0]
	v_cndmask_b32_e32 v0, v13, v175, vcc
	v_cndmask_b32_e32 v13, v15, v33, vcc
	v_cndmask_b32_e32 v14, v14, v32, vcc
	v_cndmask_b32_e32 v15, v29, v179, vcc
	v_cndmask_b32_e32 v27, v28, v178, vcc
	v_cndmask_b32_e32 v28, v31, v177, vcc
	v_cndmask_b32_e32 v29, v30, v176, vcc
	v_med3_f32 v14, v14, s63, v193
	v_med3_f32 v13, v13, s63, v193
	v_mov_b32_e32 v32, v1
	v_cvt_pk_fp8_f32 v32, v14, v13
	v_med3_f32 v13, v29, s63, v193
	v_med3_f32 v14, v28, s63, v193
	v_mov_b32_e32 v33, v1
	v_cvt_pk_fp8_f32 v33, v13, v14
	v_cndmask_b32_e32 v12, v12, v174, vcc
	v_med3_f32 v12, v12, s63, v193
	v_med3_f32 v0, v0, s63, v193
	v_cvt_pk_fp8_f32 v32, v12, v0 op_sel:[0,0,1]
	v_med3_f32 v0, v27, s63, v193
	v_med3_f32 v12, v15, s63, v193
	v_pk_mul_f32 v[14:15], v[42:43], v[6:7]
	v_cvt_pk_fp8_f32 v33, v0, v12 op_sel:[0,0,1]
	v_pk_mul_f32 v[12:13], v[44:45], v[8:9]
	v_pk_fma_f32 v[14:15], v[58:59], v[2:3], v[14:15] neg_lo:[0,0,1] neg_hi:[0,0,1]
	v_pk_mul_f32 v[6:7], v[58:59], v[6:7]
	v_pk_fma_f32 v[12:13], v[60:61], v[4:5], v[12:13] neg_lo:[0,0,1] neg_hi:[0,0,1]
	v_pk_mul_f32 v[8:9], v[60:61], v[8:9]
	v_pk_fma_f32 v[2:3], v[42:43], v[2:3], v[6:7]
	v_pk_mul_f32 v[6:7], v[14:15], s[30:31] op_sel_hi:[1,0]
	v_pk_fma_f32 v[4:5], v[44:45], v[4:5], v[8:9]
; __device__ __forceinline__ unsigned cvt_fp8x4_sat(float a, float b, float c, float d) { return cvt_fp8x4(__builtin_amdgcn_fmed3f(a, -448.f, 448.f), __builtin_amdgcn_fmed3f(b, -448.f, 448.f), __builtin_amdgcn_fmed3f(c, -448.f, 448.f), __builtin_amdgcn_fmed3f(d, -448.f, 448.f)); }
;     __device__ __forceinline__ void operator()(const f32x4 (&acc)[2][2][4][2], const Unit& u, int wr, int wc, int fr, int fq, const LAS unsigned char* epl) const {
;     ...
;         bf16_t* base = Q + (size_t)t * qkv_stride;
; #pragma unroll
;         for (int ai = 0; ai < 2; ++ai)
; #pragma unroll
;             for (int m = 0; m < 4; ++m) {
;                 const int row = u.pm * BM + ai * HALF + wr * 64 + m * 16 + fr;
;                 f32x4 cs = (f32x4){1.f, 1.f, 1.f, 1.f}, sn = (f32x4){0.f, 0.f, 0.f, 0.f};
;                 if (row >= NCTX) { const int tp = (row - NCTX) & (SEQ - 1); const int pos = (wc & 1) ? (tp & 63) : (tp >> 6);
;                     cs = *(const f32x4*)(ropec + pos * 16 + 4 * fq); sn = *(const f32x4*)(ropes + pos * 16 + 4 * fq); }
; #pragma unroll
;                 for (int bj = 0; bj < 2; ++bj) { const f32x4 x1 = acc[ai][bj][m][0], x2 = acc[ai][bj][m][1];
;                     f32x4 o1 = x1 * cs - x2 * sn, o2 = x1 * sn + x2 * cs;
;                     if (t == 0) { o1 = o1 * QK_PRESCALE; o2 = o2 * QK_PRESCALE; }
;                     { unsigned char* r8 = (unsigned char*)base + (size_t)row * DM + colt + wc * 32 + 4 * fq + bj * HALF;
;                         *(unsigned*)r8 = cvt_fp8x4_sat(o1[0], o1[1], o1[2], o1[3]); *(unsigned*)(r8 + 16) = cvt_fp8x4_sat(o2[0], o2[1], o2[2], o2[3]); } } }
	v_pk_mul_f32 v[8:9], v[12:13], s[30:31] op_sel_hi:[1,0]
	v_pk_mul_f32 v[28:29], v[2:3], s[30:31] op_sel_hi:[1,0]
	v_cndmask_b32_e32 v7, v15, v7, vcc
	v_cndmask_b32_e32 v6, v14, v6, vcc
	v_cndmask_b32_e32 v0, v13, v9, vcc
	v_cndmask_b32_e32 v3, v3, v29, vcc
	v_cndmask_b32_e32 v2, v2, v28, vcc
	v_med3_f32 v6, v6, s63, v193
	v_med3_f32 v7, v7, s63, v193
	v_mov_b32_e32 v9, v1
	v_cvt_pk_fp8_f32 v9, v6, v7
	v_med3_f32 v2, v2, s63, v193
	v_med3_f32 v3, v3, s63, v193
	v_mov_b32_e32 v6, v1
	v_cvt_pk_fp8_f32 v6, v2, v3
	v_pk_mul_f32 v[30:31], v[4:5], s[30:31] op_sel_hi:[1,0]
	v_cndmask_b32_e32 v8, v12, v8, vcc
	v_ashrrev_i32_e32 v11, 31, v10
	v_cndmask_b32_e32 v5, v5, v31, vcc
	v_cndmask_b32_e32 v4, v4, v30, vcc
	v_med3_f32 v8, v8, s63, v193
	v_med3_f32 v0, v0, s63, v193
	v_lshlrev_b64 v[10:11], 10, v[10:11]
	v_cvt_pk_fp8_f32 v9, v8, v0 op_sel:[0,0,1]
	v_med3_f32 v0, v4, s63, v193
	v_med3_f32 v2, v5, s63, v193
	v_lshl_add_u64 v[10:11], v[22:23], 0, v[10:11]
	v_cvt_pk_fp8_f32 v6, v0, v2 op_sel:[0,0,1]
	v_add_u32_e32 v4, 0xa0, v16
	global_store_dword v[10:11], v32, off
	global_store_dword v[10:11], v33, off offset:16
	global_store_dword v[10:11], v9, off offset:128
	global_store_dword v[10:11], v6, off offset:144
	v_cmp_lt_i32_e64 s[6:7], s47, v4
	v_mov_b32_e32 v6, 0
	v_mov_b32_e32 v2, 1.0
	v_mov_b32_e32 v8, 1.0
	v_mov_b32_e32 v9, 1.0
	v_mov_b32_e32 v10, 1.0
	v_mov_b32_e32 v11, 1.0
	v_mov_b32_e32 v12, 0
	v_mov_b32_e32 v13, 0
	v_mov_b32_e32 v14, 0
	v_mov_b32_e32 v15, 0
	s_and_saveexec_b64 s[0:1], s[6:7]
	s_cbranch_execz .LBB0_435
	v_add_u32_e32 v0, 0x18a0, v16
	v_bfe_u32 v0, v0, 6, 7
	v_cndmask_b32_e64 v0, v17, v0, s[2:3]
	v_lshlrev_b32_e32 v0, 6, v0
	v_add_u32_e32 v249, v250, v0
	ds_read_b128 v[8:11], v249
	ds_read_b128 v[12:15], v249 offset:8192
.LBB0_435:
	s_or_b64 exec, exec, s[0:1]
	s_waitcnt lgkmcnt(0)
	v_pk_mul_f32 v[30:31], v[70:71], v[12:13]
	v_pk_mul_f32 v[174:175], v[86:87], v[12:13]
	v_pk_fma_f32 v[30:31], v[86:87], v[8:9], v[30:31] neg_lo:[0,0,1] neg_hi:[0,0,1]
	v_pk_fma_f32 v[174:175], v[70:71], v[8:9], v[174:175]
	v_pk_mul_f32 v[176:177], v[30:31], s[30:31] op_sel_hi:[1,0]
	v_pk_mul_f32 v[28:29], v[72:73], v[14:15]
	v_pk_mul_f32 v[180:181], v[174:175], s[30:31] op_sel_hi:[1,0]
	v_cndmask_b32_e32 v7, v31, v177, vcc
	v_cndmask_b32_e32 v17, v30, v176, vcc
	v_pk_fma_f32 v[28:29], v[88:89], v[10:11], v[28:29] neg_lo:[0,0,1] neg_hi:[0,0,1]
	v_cndmask_b32_e32 v30, v174, v180, vcc
	v_med3_f32 v17, v17, s63, v193
	v_med3_f32 v7, v7, s63, v193
	v_mov_b32_e32 v173, v1
	v_pk_mul_f32 v[32:33], v[88:89], v[14:15]
	v_pk_mul_f32 v[178:179], v[28:29], s[30:31] op_sel_hi:[1,0]
	v_cvt_pk_fp8_f32 v173, v17, v7
	v_med3_f32 v7, v30, s63, v193
	v_pk_mul_f32 v[30:31], v[38:39], v[12:13]
	v_pk_fma_f32 v[32:33], v[72:73], v[10:11], v[32:33]
	v_cndmask_b32_e32 v0, v29, v179, vcc
	v_cndmask_b32_e32 v29, v175, v181, vcc
	v_pk_fma_f32 v[30:31], v[54:55], v[8:9], v[30:31] neg_lo:[0,0,1] neg_hi:[0,0,1]
	v_pk_mul_f32 v[12:13], v[54:55], v[12:13]
	v_pk_mul_f32 v[198:199], v[32:33], s[30:31] op_sel_hi:[1,0]
	v_cndmask_b32_e32 v3, v28, v178, vcc
	v_med3_f32 v17, v29, s63, v193
	v_mov_b32_e32 v176, v1
	v_pk_fma_f32 v[8:9], v[38:39], v[8:9], v[12:13]
	v_pk_mul_f32 v[12:13], v[30:31], s[30:31] op_sel_hi:[1,0]
	v_cndmask_b32_e32 v27, v33, v199, vcc
	v_cndmask_b32_e32 v28, v32, v198, vcc
	v_med3_f32 v3, v3, s63, v193
	v_med3_f32 v0, v0, s63, v193
	v_cvt_pk_fp8_f32 v176, v7, v17
	v_pk_mul_f32 v[32:33], v[8:9], s[30:31] op_sel_hi:[1,0]
	v_cndmask_b32_e32 v7, v31, v13, vcc
	v_cndmask_b32_e32 v12, v30, v12, vcc
	v_cvt_pk_fp8_f32 v173, v3, v0 op_sel:[0,0,1]
	v_med3_f32 v0, v28, s63, v193
	v_pk_mul_f32 v[28:29], v[40:41], v[14:15]
	v_cndmask_b32_e32 v9, v9, v33, vcc
	v_cndmask_b32_e32 v8, v8, v32, vcc
	v_med3_f32 v12, v12, s63, v193
	v_med3_f32 v7, v7, s63, v193
	v_mov_b32_e32 v13, v1
	v_pk_fma_f32 v[28:29], v[56:57], v[10:11], v[28:29] neg_lo:[0,0,1] neg_hi:[0,0,1]
	v_pk_mul_f32 v[14:15], v[56:57], v[14:15]
	v_cvt_pk_fp8_f32 v13, v12, v7
	v_med3_f32 v7, v8, s63, v193
	v_med3_f32 v8, v9, s63, v193
	v_mov_b32_e32 v9, v1
	v_med3_f32 v3, v27, s63, v193
	v_pk_fma_f32 v[10:11], v[40:41], v[10:11], v[14:15]
	v_pk_mul_f32 v[14:15], v[28:29], s[30:31] op_sel_hi:[1,0]
	v_cvt_pk_fp8_f32 v9, v7, v8
	v_cvt_pk_fp8_f32 v176, v0, v3 op_sel:[0,0,1]
	v_pk_mul_f32 v[174:175], v[10:11], s[30:31] op_sel_hi:[1,0]
	v_cndmask_b32_e32 v0, v29, v15, vcc
	v_cndmask_b32_e32 v3, v28, v14, vcc
	v_ashrrev_i32_e32 v5, 31, v4
	v_cndmask_b32_e32 v11, v11, v175, vcc
	v_cndmask_b32_e32 v10, v10, v174, vcc
	v_med3_f32 v3, v3, s63, v193
	v_med3_f32 v0, v0, s63, v193
	v_lshlrev_b64 v[4:5], 10, v[4:5]
	v_cvt_pk_fp8_f32 v13, v3, v0 op_sel:[0,0,1]
	v_med3_f32 v0, v10, s63, v193
	v_med3_f32 v3, v11, s63, v193
	v_lshl_add_u64 v[4:5], v[22:23], 0, v[4:5]
	v_cvt_pk_fp8_f32 v9, v0, v3 op_sel:[0,0,1]
	v_add_u32_e32 v10, 0xb0, v16
	global_store_dword v[4:5], v173, off
	global_store_dword v[4:5], v176, off offset:16
	global_store_dword v[4:5], v13, off offset:128
	global_store_dword v[4:5], v9, off offset:144
	v_cmp_lt_i32_e64 s[6:7], s47, v10
	v_mov_b32_e32 v3, 1.0
	v_mov_b32_e32 v4, 1.0
	v_mov_b32_e32 v5, 1.0
	v_mov_b32_e32 v7, 0
	v_mov_b32_e32 v8, 0
	v_mov_b32_e32 v9, 0
	s_and_saveexec_b64 s[0:1], s[6:7]
	s_cbranch_execz .LBB0_437
	v_add_u32_e32 v0, 0x18b0, v16
	v_bfe_u32 v0, v0, 6, 7
	v_cndmask_b32_e64 v0, v26, v0, s[2:3]
	v_lshlrev_b32_e32 v0, 6, v0
	v_add_u32_e32 v249, v250, v0
	ds_read_b128 v[2:5], v249
	ds_read_b128 v[6:9], v249 offset:8192
; __device__ __forceinline__ unsigned cvt_fp8x4_sat(float a, float b, float c, float d) { return cvt_fp8x4(__builtin_amdgcn_fmed3f(a, -448.f, 448.f), __builtin_amdgcn_fmed3f(b, -448.f, 448.f), __builtin_amdgcn_fmed3f(c, -448.f, 448.f), __builtin_amdgcn_fmed3f(d, -448.f, 448.f)); }
;     __device__ __forceinline__ void operator()(const f32x4 (&acc)[2][2][4][2], const Unit& u, int wr, int wc, int fr, int fq, const LAS unsigned char* epl) const {
;     ...
;         bf16_t* base = Q + (size_t)t * qkv_stride;
; #pragma unroll
;         for (int ai = 0; ai < 2; ++ai)
; #pragma unroll
;             for (int m = 0; m < 4; ++m) {
;                 const int row = u.pm * BM + ai * HALF + wr * 64 + m * 16 + fr;
;                 f32x4 cs = (f32x4){1.f, 1.f, 1.f, 1.f}, sn = (f32x4){0.f, 0.f, 0.f, 0.f};
;                 if (row >= NCTX) { const int tp = (row - NCTX) & (SEQ - 1); const int pos = (wc & 1) ? (tp & 63) : (tp >> 6);
;                     cs = *(const f32x4*)(ropec + pos * 16 + 4 * fq); sn = *(const f32x4*)(ropes + pos * 16 + 4 * fq); }
; #pragma unroll
;                 for (int bj = 0; bj < 2; ++bj) { const f32x4 x1 = acc[ai][bj][m][0], x2 = acc[ai][bj][m][1];
;                     f32x4 o1 = x1 * cs - x2 * sn, o2 = x1 * sn + x2 * cs;
;                     if (t == 0) { o1 = o1 * QK_PRESCALE; o2 = o2 * QK_PRESCALE; }
;                     { unsigned char* r8 = (unsigned char*)base + (size_t)row * DM + colt + wc * 32 + 4 * fq + bj * HALF;
;                         *(unsigned*)r8 = cvt_fp8x4_sat(o1[0], o1[1], o1[2], o1[3]); *(unsigned*)(r8 + 16) = cvt_fp8x4_sat(o2[0], o2[1], o2[2], o2[3]); } } }
.LBB0_437:
	s_or_b64 exec, exec, s[0:1]
	v_ashrrev_i32_e32 v11, 31, v10
	s_waitcnt lgkmcnt(0)
	v_pk_mul_f32 v[12:13], v[68:69], v[8:9]
	v_pk_mul_f32 v[14:15], v[66:67], v[6:7]
	v_lshlrev_b64 v[10:11], 10, v[10:11]
	v_pk_fma_f32 v[14:15], v[82:83], v[2:3], v[14:15] neg_lo:[0,0,1] neg_hi:[0,0,1]
	v_pk_fma_f32 v[12:13], v[84:85], v[4:5], v[12:13] neg_lo:[0,0,1] neg_hi:[0,0,1]
	v_pk_mul_f32 v[16:17], v[84:85], v[8:9]
	v_pk_mul_f32 v[18:19], v[82:83], v[6:7]
	v_lshl_add_u64 v[10:11], v[22:23], 0, v[10:11]
	v_pk_fma_f32 v[18:19], v[66:67], v[2:3], v[18:19]
	v_pk_fma_f32 v[16:17], v[68:69], v[4:5], v[16:17]
	v_pk_mul_f32 v[20:21], v[14:15], s[30:31] op_sel_hi:[1,0]
	v_pk_mul_f32 v[22:23], v[12:13], s[30:31] op_sel_hi:[1,0]
	v_pk_mul_f32 v[26:27], v[18:19], s[30:31] op_sel_hi:[1,0]
	v_pk_mul_f32 v[28:29], v[16:17], s[30:31] op_sel_hi:[1,0]
	v_cndmask_b32_e32 v0, v13, v23, vcc
	v_cndmask_b32_e32 v13, v15, v21, vcc
	v_cndmask_b32_e32 v14, v14, v20, vcc
	v_cndmask_b32_e32 v15, v17, v29, vcc
	v_cndmask_b32_e32 v17, v19, v27, vcc
	v_cndmask_b32_e32 v18, v18, v26, vcc
	v_med3_f32 v14, v14, s63, v193
	v_med3_f32 v13, v13, s63, v193
	v_mov_b32_e32 v20, v1
	v_cvt_pk_fp8_f32 v20, v14, v13
	v_med3_f32 v13, v18, s63, v193
	v_med3_f32 v14, v17, s63, v193
	v_mov_b32_e32 v21, v1
	v_cvt_pk_fp8_f32 v21, v13, v14
	v_cndmask_b32_e32 v12, v12, v22, vcc
	v_cndmask_b32_e32 v16, v16, v28, vcc
	v_med3_f32 v12, v12, s63, v193
	v_med3_f32 v0, v0, s63, v193
	v_cvt_pk_fp8_f32 v20, v12, v0 op_sel:[0,0,1]
	v_med3_f32 v0, v16, s63, v193
	v_med3_f32 v12, v15, s63, v193
	v_pk_mul_f32 v[14:15], v[34:35], v[6:7]
	v_cvt_pk_fp8_f32 v21, v0, v12 op_sel:[0,0,1]
	v_pk_mul_f32 v[12:13], v[36:37], v[8:9]
	v_pk_fma_f32 v[14:15], v[50:51], v[2:3], v[14:15] neg_lo:[0,0,1] neg_hi:[0,0,1]
	v_pk_mul_f32 v[6:7], v[50:51], v[6:7]
	v_pk_fma_f32 v[12:13], v[52:53], v[4:5], v[12:13] neg_lo:[0,0,1] neg_hi:[0,0,1]
	v_pk_mul_f32 v[8:9], v[52:53], v[8:9]
	v_pk_fma_f32 v[2:3], v[34:35], v[2:3], v[6:7]
	v_pk_mul_f32 v[6:7], v[14:15], s[30:31] op_sel_hi:[1,0]
	v_pk_fma_f32 v[4:5], v[36:37], v[4:5], v[8:9]
	v_pk_mul_f32 v[8:9], v[12:13], s[30:31] op_sel_hi:[1,0]
	v_pk_mul_f32 v[16:17], v[2:3], s[30:31] op_sel_hi:[1,0]
	v_cndmask_b32_e32 v7, v15, v7, vcc
	v_cndmask_b32_e32 v6, v14, v6, vcc
	v_cndmask_b32_e32 v0, v13, v9, vcc
	v_cndmask_b32_e32 v3, v3, v17, vcc
	v_cndmask_b32_e32 v2, v2, v16, vcc
	v_med3_f32 v6, v6, s63, v193
	v_med3_f32 v7, v7, s63, v193
	v_mov_b32_e32 v9, v1
	v_cvt_pk_fp8_f32 v9, v6, v7
	v_med3_f32 v2, v2, s63, v193
	v_med3_f32 v3, v3, s63, v193
	v_mov_b32_e32 v6, v1
	v_cvt_pk_fp8_f32 v6, v2, v3
	v_pk_mul_f32 v[18:19], v[4:5], s[30:31] op_sel_hi:[1,0]
	v_cndmask_b32_e32 v8, v12, v8, vcc
	v_cndmask_b32_e32 v5, v5, v19, vcc
	v_cndmask_b32_e32 v4, v4, v18, vcc
	v_med3_f32 v8, v8, s63, v193
	v_med3_f32 v0, v0, s63, v193
	v_cvt_pk_fp8_f32 v9, v8, v0 op_sel:[0,0,1]
	v_med3_f32 v0, v4, s63, v193
	v_med3_f32 v2, v5, s63, v193
	v_cvt_pk_fp8_f32 v6, v0, v2 op_sel:[0,0,1]
	global_store_dword v[10:11], v20, off
	global_store_dword v[10:11], v21, off offset:16
	global_store_dword v[10:11], v9, off offset:128
	global_store_dword v[10:11], v6, off offset:144
	s_branch .LBB0_420

; __global__ void __launch_bounds__(NWAVES * 64, 2) fwd_kernel(Args args) {
;     extern __shared__ __attribute__((aligned(16))) unsigned char lds[];
	.amdhsa_kernel _Z10fwd_kernel4Args
		.amdhsa_group_segment_fixed_size 16384
		.amdhsa_private_segment_fixed_size 0
		.amdhsa_kernarg_size 488
		.amdhsa_user_sgpr_count 2
		.amdhsa_user_sgpr_dispatch_ptr 0
		.amdhsa_user_sgpr_queue_ptr 0
		.amdhsa_user_sgpr_kernarg_segment_ptr 1
		.amdhsa_user_sgpr_dispatch_id 0
		.amdhsa_user_sgpr_kernarg_preload_length 0
		.amdhsa_user_sgpr_kernarg_preload_offset 0
		.amdhsa_user_sgpr_private_segment_size 0
		.amdhsa_uses_dynamic_stack 0
		.amdhsa_enable_private_segment 0
		.amdhsa_system_sgpr_workgroup_id_x 1
		.amdhsa_system_sgpr_workgroup_id_y 0
		.amdhsa_system_sgpr_workgroup_id_z 0
		.amdhsa_system_sgpr_workgroup_info 0
		.amdhsa_system_vgpr_workitem_id 0
		.amdhsa_next_free_vgpr 256
		.amdhsa_next_free_sgpr 100
		.amdhsa_accum_offset 256
		.amdhsa_reserve_vcc 1
		.amdhsa_float_round_mode_32 0
		.amdhsa_float_round_mode_16_64 0
		.amdhsa_float_denorm_mode_32 3
		.amdhsa_float_denorm_mode_16_64 3
		.amdhsa_dx10_clamp 1
		.amdhsa_ieee_mode 1
		.amdhsa_fp16_overflow 0
		.amdhsa_tg_split 0
		.amdhsa_exception_fp_ieee_invalid_op 0
		.amdhsa_exception_fp_denorm_src 0
		.amdhsa_exception_fp_ieee_div_zero 0
		.amdhsa_exception_fp_ieee_overflow 0
		.amdhsa_exception_fp_ieee_underflow 0
		.amdhsa_exception_fp_ieee_inexact 0
		.amdhsa_exception_int_div_zero 0
	.end_amdhsa_kernel

; __global__ void __launch_bounds__(NWAVES * 64, 2) fwd_kernel(Args args) {
;     extern __shared__ __attribute__((aligned(16))) unsigned char lds[];
amdhsa.kernels:
  - .agpr_count:     0
    .args:
      - .offset:         0
        .size:           232
        .value_kind:     by_value
      - .offset:         232
        .size:           4
        .value_kind:     hidden_block_count_x
      - .offset:         236
        .size:           4
        .value_kind:     hidden_block_count_y
      - .offset:         240
        .size:           4
        .value_kind:     hidden_block_count_z
      - .offset:         244
        .size:           2
        .value_kind:     hidden_group_size_x
      - .offset:         246
        .size:           2
        .value_kind:     hidden_group_size_y
      - .offset:         248
        .size:           2
        .value_kind:     hidden_group_size_z
      - .offset:         250
        .size:           2
        .value_kind:     hidden_remainder_x
      - .offset:         252
        .size:           2
        .value_kind:     hidden_remainder_y
      - .offset:         254
        .size:           2
        .value_kind:     hidden_remainder_z
      - .offset:         272
        .size:           8
        .value_kind:     hidden_global_offset_x
      - .offset:         280
        .size:           8
        .value_kind:     hidden_global_offset_y
      - .offset:         288
        .size:           8
        .value_kind:     hidden_global_offset_z
      - .offset:         296
        .size:           2
        .value_kind:     hidden_grid_dims
      - .offset:         352
        .size:           4
        .value_kind:     hidden_dynamic_lds_size
    .group_segment_fixed_size: 16384
    .kernarg_segment_align: 8
    .kernarg_segment_size: 488
    .language:       OpenCL C
    .language_version:
      - 2
      - 0
    .max_flat_workgroup_size: 512
    .name:           _Z10fwd_kernel4Args
    .private_segment_fixed_size: 0
    .sgpr_count:     106
    .sgpr_spill_count: 44
    .symbol:         _Z10fwd_kernel4Args.kd
    .uniform_work_group_size: 1
    .uses_dynamic_stack: false
    .vgpr_count:     256
    .vgpr_spill_count: 0
    .wavefront_size: 64
